# G1 GEMM: peel first K-loop iteration with C=0 instead of zeroing 128 accumulator VGPRs per unit
# baseline (speedup 1.0000x reference)
; #define PG8_STAGE(bufoff, gbase, voff) do { _Pragma("unroll") for (int _i = 0; _i < 2; ++_i) \
;         __builtin_amdgcn_global_load_lds((const unsigned*)((const char*)(gbase) + (voff)[_i]), (PG8_LAS unsigned*)(lds + (bufoff) + ldsw + _i * 8192), 16, 0, 0); } while (0)
; #define PG8_LDA(dst, b, h) do { _Pragma("unroll") for (int m = 0; m < 4; ++m) _Pragma("unroll") for (int k = 0; k < 2; ++k) dst[m][k] = *(const PG8_LAS bf16x8*)(lds + PG8_SA(b, h) + aoff + m * 2048 + k * 1024); } while (0)
; #define PG8_LDB(dst, b, h) do { _Pragma("unroll") for (int n = 0; n < 2; ++n) _Pragma("unroll") for (int k = 0; k < 2; ++k) dst[n][k] = *(const PG8_LAS bf16x8*)(lds + PG8_SB(b, h) + boff + n * 2048 + k * 1024); } while (0)
; #define PG8_WAIT_V(n) asm volatile("s_waitcnt vmcnt(" #n ")" ::: "memory")
; #define PG8_WAIT_L(n) asm volatile("s_waitcnt lgkmcnt(" #n ")" ::: "memory")
; #define PG8_BAR __builtin_amdgcn_s_barrier()
; #define PG8_SCHED __builtin_amdgcn_sched_barrier(0)
; template <class Epi, class Sched, bool ALIGN_EPI = false, bool SP2 = false>
; __device__ __forceinline__ void gemm_phase(PG8_LAS unsigned char* lds, const Gemm g, const Sched& S, const Epi& E, const int tid) {
;     ...
;         const char* nA = has_next ? (const char*)g.A + (size_t)nxt.pm * tstep : cA; const char* nB = has_next ? (const char*)g.Bt + (size_t)nxt.pn * tstep : cB;
;         for (int t = 0; t < nt; t += 2) {
;             const bool last = (t == nt - 2);
;             const char* a1 = cA + (size_t)(t + 1) * kstep;
;             const char* a2 = last ? nA : cA + (size_t)(t + 2) * kstep; const char* b2 = last ? nB : cB + (size_t)(t + 2) * kstep;
;             const char* a3 = a2 + kstep; const char* b3 = b2 + kstep;
;             if (last && has_next) S.a_ready(nxt);
;             if constexpr (SP2) {
;             PG8_LDB(B0, 0, 0); PG8_LDB(B1, 0, 1); PG8_SCHED; PG8_LDA(At, 0, 0); PG8_STAGE(PG8_SA(1, 1), a1 + hstep, voffA);
;             PG8_WAIT_V(8); PG8_WAIT_L(0); PG8_BAR; PG8_MMA(0, 0, At, B0); PG8_MMA(0, 1, At, B1); PG8_BAR; PG8_SCHED;
;             PG8_LDA(At, 0, 1); PG8_STAGE(PG8_SB(0, 0), b2, voffB); PG8_STAGE(PG8_SB(0, 1), b2, voffB1); PG8_STAGE(PG8_SA(0, 0), a2, voffA);
;             PG8_WAIT_V(8); PG8_WAIT_L(0); PG8_BAR; PG8_MMA(1, 0, At, B0); PG8_MMA(1, 1, At, B1); PG8_BAR; PG8_SCHED;
.LBB0_726:
	s_ashr_i32 s11, s10, 31
	s_lshl_b64 s[12:13], s[10:11], 19
	s_add_u32 s12, s38, s12
	s_addc_u32 s13, s39, s13
	s_and_b64 s[14:15], s[2:3], exec
	s_cselect_b32 s11, s13, s47
	s_cselect_b32 s59, s12, s46
	s_ashr_i32 s9, s8, 31
	s_lshl_b64 s[14:15], s[8:9], 19
	s_add_u32 s14, s40, s14
	s_addc_u32 s15, s41, s15
	s_and_b64 s[36:37], s[2:3], exec
	s_cselect_b32 s9, s15, s53
	s_cselect_b32 s60, s14, s52
	s_add_u32 s46, s46, 0x40080
	s_addc_u32 s47, s47, 0
	s_add_u32 s52, s52, 0x100
	s_addc_u32 s53, s53, 0
	s_mov_b32 s62, -2
	s_add_u32 s36, s46, 0xfffc0080
	s_addc_u32 s37, s47, -1
	s_add_i32 s63, 0, 0x10000
	s_cmp_eq_u32 s62, 12
	s_cselect_b32 s37, s11, s37
	s_cselect_b32 s36, s59, s36
	v_add_u32_e32 v148, s63, v151
	s_cselect_b32 s73, s9, s53
	s_cselect_b32 s72, s60, s52
	s_add_i32 s68, 0, 0x14000
	ds_read_b128 v[144:147], v148
	ds_read_b128 v[156:159], v148 offset:1024
	ds_read_b128 v[160:163], v148 offset:2048
	ds_read_b128 v[164:167], v148 offset:3072
	v_add_u32_e32 v148, s68, v151
	ds_read_b128 v[168:171], v148
	ds_read_b128 v[172:175], v148 offset:1024
	ds_read_b128 v[176:179], v148 offset:2048
	ds_read_b128 v[180:183], v148 offset:3072
	v_lshl_add_u64 v[148:149], s[46:47], 0, v[140:141]
	s_add_i32 m0, s43, 0xc000
	ds_read_b128 v[184:187], v154
	ds_read_b128 v[188:191], v154 offset:1024
	ds_read_b128 v[192:195], v154 offset:2048
	ds_read_b128 v[196:199], v154 offset:3072
	ds_read_b128 v[212:215], v154 offset:4096
	ds_read_b128 v[216:219], v154 offset:5120
	ds_read_b128 v[220:223], v154 offset:6144
	ds_read_b128 v[224:227], v154 offset:7168
	global_load_lds_dwordx4 v[148:149], off
	v_lshl_add_u64 v[148:149], s[46:47], 0, v[142:143]
	s_add_i32 m0, s43, 0xe000
	s_nop 0
	global_load_lds_dwordx4 v[148:149], off
	s_waitcnt vmcnt(8)
	s_waitcnt lgkmcnt(0)
	s_barrier
	s_setprio 1
	s_waitcnt lgkmcnt(0)
	v_mfma_f32_16x16x32_bf16 v[128:131], v[144:147], v[184:187], 0
	v_mfma_f32_16x16x32_bf16 v[120:123], v[160:163], v[184:187], 0
	v_mfma_f32_16x16x32_bf16 v[112:115], v[144:147], v[192:195], 0
	v_mfma_f32_16x16x32_bf16 v[104:107], v[160:163], v[192:195], 0
	v_mfma_f32_16x16x32_bf16 v[96:99], v[144:147], v[212:215], 0
	v_mfma_f32_16x16x32_bf16 v[88:91], v[160:163], v[212:215], 0
	v_mfma_f32_16x16x32_bf16 v[80:83], v[144:147], v[220:223], 0
	v_mfma_f32_16x16x32_bf16 v[72:75], v[160:163], v[220:223], 0
	v_mfma_f32_16x16x32_bf16 v[128:131], v[156:159], v[188:191], v[128:131]
	v_mfma_f32_16x16x32_bf16 v[120:123], v[164:167], v[188:191], v[120:123]
	v_mfma_f32_16x16x32_bf16 v[112:115], v[156:159], v[196:199], v[112:115]
	v_mfma_f32_16x16x32_bf16 v[104:107], v[164:167], v[196:199], v[104:107]
	v_mfma_f32_16x16x32_bf16 v[96:99], v[156:159], v[216:219], v[96:99]
	v_mfma_f32_16x16x32_bf16 v[88:91], v[164:167], v[216:219], v[88:91]
	v_mfma_f32_16x16x32_bf16 v[80:83], v[156:159], v[224:227], v[80:83]
	v_mfma_f32_16x16x32_bf16 v[72:75], v[164:167], v[224:227], v[72:75]
	s_setprio 0
	s_setprio 1
	v_mfma_f32_16x16x32_bf16 v[124:127], v[168:171], v[184:187], 0
	v_mfma_f32_16x16x32_bf16 v[116:119], v[176:179], v[184:187], 0
	v_mfma_f32_16x16x32_bf16 v[108:111], v[168:171], v[192:195], 0
	v_mfma_f32_16x16x32_bf16 v[100:103], v[176:179], v[192:195], 0
	v_mfma_f32_16x16x32_bf16 v[92:95], v[168:171], v[212:215], 0
	v_mfma_f32_16x16x32_bf16 v[84:87], v[176:179], v[212:215], 0
	v_mfma_f32_16x16x32_bf16 v[76:79], v[168:171], v[220:223], 0
	v_mfma_f32_16x16x32_bf16 v[68:71], v[176:179], v[220:223], 0
	v_mfma_f32_16x16x32_bf16 v[124:127], v[172:175], v[188:191], v[124:127]
	v_mfma_f32_16x16x32_bf16 v[116:119], v[180:183], v[188:191], v[116:119]
	v_mfma_f32_16x16x32_bf16 v[108:111], v[172:175], v[196:199], v[108:111]
	v_mfma_f32_16x16x32_bf16 v[100:103], v[180:183], v[196:199], v[100:103]
	v_mfma_f32_16x16x32_bf16 v[92:95], v[172:175], v[216:219], v[92:95]
	v_mfma_f32_16x16x32_bf16 v[84:87], v[180:183], v[216:219], v[84:87]
	v_mfma_f32_16x16x32_bf16 v[76:79], v[172:175], v[224:227], v[76:79]
	v_mfma_f32_16x16x32_bf16 v[68:71], v[180:183], v[224:227], v[68:71]
	s_setprio 0
	s_barrier
	s_add_i32 s63, s63, s33
	v_lshl_add_u64 v[148:149], s[72:73], 0, v[2:3]
	s_mov_b32 m0, s63
	ds_read_b128 v[184:187], v154 offset:16384
	ds_read_b128 v[188:191], v154 offset:17408
	ds_read_b128 v[192:195], v154 offset:18432
	ds_read_b128 v[196:199], v154 offset:19456
	ds_read_b128 v[212:215], v154 offset:20480
	ds_read_b128 v[216:219], v154 offset:21504
	ds_read_b128 v[220:223], v154 offset:22528
	ds_read_b128 v[224:227], v154 offset:23552
	global_load_lds_dwordx4 v[148:149], off
	v_lshl_add_u64 v[200:201], s[72:73], 0, v[132:133]
	s_add_i32 m0, s63, 0x2000
	s_add_i32 s63, s68, s33
	global_load_lds_dwordx4 v[200:201], off
	v_lshl_add_u64 v[202:203], s[72:73], 0, v[136:137]
	s_mov_b32 m0, s63
	v_lshl_add_u64 v[204:205], s[72:73], 0, v[0:1]
	global_load_lds_dwordx4 v[202:203], off
	s_add_i32 m0, s63, 0x2000
	v_lshl_add_u64 v[208:209], s[36:37], 0, v[138:139]
	global_load_lds_dwordx4 v[204:205], off
	s_mov_b32 m0, s43
	v_lshl_add_u64 v[210:211], s[36:37], 0, v[134:135]
	global_load_lds_dwordx4 v[208:209], off
	s_mov_b32 m0, s45
	s_nop 0
	global_load_lds_dwordx4 v[210:211], off
	s_waitcnt vmcnt(8)
	s_waitcnt lgkmcnt(0)
	s_barrier
; #define PG8_STAGE(bufoff, gbase, voff) do { _Pragma("unroll") for (int _i = 0; _i < 2; ++_i) \
;         __builtin_amdgcn_global_load_lds((const unsigned*)((const char*)(gbase) + (voff)[_i]), (PG8_LAS unsigned*)(lds + (bufoff) + ldsw + _i * 8192), 16, 0, 0); } while (0)
; #define PG8_LDA(dst, b, h) do { _Pragma("unroll") for (int m = 0; m < 4; ++m) _Pragma("unroll") for (int k = 0; k < 2; ++k) dst[m][k] = *(const PG8_LAS bf16x8*)(lds + PG8_SA(b, h) + aoff + m * 2048 + k * 1024); } while (0)
; #define PG8_LDB(dst, b, h) do { _Pragma("unroll") for (int n = 0; n < 2; ++n) _Pragma("unroll") for (int k = 0; k < 2; ++k) dst[n][k] = *(const PG8_LAS bf16x8*)(lds + PG8_SB(b, h) + boff + n * 2048 + k * 1024); } while (0)
; #define PG8_MMA(ai, bj, At, Bt) do { __builtin_amdgcn_s_setprio(1); _Pragma("unroll") for (int m = 0; m < 4; ++m) _Pragma("unroll") for (int n = 0; n < 2; ++n) _Pragma("unroll") for (int k = 0; k < 2; ++k) \
;         acc[ai][bj][m][n] = __builtin_amdgcn_mfma_f32_16x16x32_bf16(Bt[n][k], At[m][k], acc[ai][bj][m][n], 0, 0, 0); __builtin_amdgcn_s_setprio(0); } while (0)
; #define PG8_WAIT_V(n) asm volatile("s_waitcnt vmcnt(" #n ")" ::: "memory")
; #define PG8_WAIT_L(n) asm volatile("s_waitcnt lgkmcnt(" #n ")" ::: "memory")
; #define PG8_BAR __builtin_amdgcn_s_barrier()
; #define PG8_SCHED __builtin_amdgcn_sched_barrier(0)
; template <class Epi, class Sched, bool ALIGN_EPI = false, bool SP2 = false>
; __device__ __forceinline__ void gemm_phase(PG8_LAS unsigned char* lds, const Gemm g, const Sched& S, const Epi& E, const int tid) {
;     ...
;             PG8_LDA(At, 0, 1); PG8_STAGE(PG8_SB(0, 0), b2, voffB); PG8_STAGE(PG8_SB(0, 1), b2, voffB1); PG8_STAGE(PG8_SA(0, 0), a2, voffA);
;             PG8_WAIT_V(8); PG8_WAIT_L(0); PG8_BAR; PG8_MMA(1, 0, At, B0); PG8_MMA(1, 1, At, B1); PG8_BAR; PG8_SCHED;
;             PG8_LDB(B0, 1, 0); PG8_LDB(B1, 1, 1); PG8_SCHED; PG8_LDA(At, 1, 0); PG8_STAGE(PG8_SA(0, 1), a2 + hstep, voffA);
;             PG8_WAIT_V(8); PG8_WAIT_L(0); PG8_BAR; PG8_MMA(0, 0, At, B0); PG8_MMA(0, 1, At, B1); PG8_BAR; PG8_SCHED;
	s_setprio 1
	s_waitcnt lgkmcnt(0)
	v_mfma_f32_16x16x32_bf16 v[64:67], v[144:147], v[184:187], 0
	v_mfma_f32_16x16x32_bf16 v[56:59], v[160:163], v[184:187], 0
	v_mfma_f32_16x16x32_bf16 v[48:51], v[144:147], v[192:195], 0
	v_mfma_f32_16x16x32_bf16 v[40:43], v[160:163], v[192:195], 0
	v_mfma_f32_16x16x32_bf16 v[32:35], v[144:147], v[212:215], 0
	v_mfma_f32_16x16x32_bf16 v[24:27], v[160:163], v[212:215], 0
	v_mfma_f32_16x16x32_bf16 v[16:19], v[144:147], v[220:223], 0
	v_mfma_f32_16x16x32_bf16 v[8:11], v[160:163], v[220:223], 0
	v_mfma_f32_16x16x32_bf16 v[64:67], v[156:159], v[188:191], v[64:67]
	v_mfma_f32_16x16x32_bf16 v[56:59], v[164:167], v[188:191], v[56:59]
	v_mfma_f32_16x16x32_bf16 v[48:51], v[156:159], v[196:199], v[48:51]
	v_mfma_f32_16x16x32_bf16 v[40:43], v[164:167], v[196:199], v[40:43]
	v_mfma_f32_16x16x32_bf16 v[32:35], v[156:159], v[216:219], v[32:35]
	v_mfma_f32_16x16x32_bf16 v[24:27], v[164:167], v[216:219], v[24:27]
	v_mfma_f32_16x16x32_bf16 v[16:19], v[156:159], v[224:227], v[16:19]
	v_mfma_f32_16x16x32_bf16 v[8:11], v[164:167], v[224:227], v[8:11]
	s_setprio 0
	s_setprio 1
	v_mfma_f32_16x16x32_bf16 v[60:63], v[168:171], v[184:187], 0
	v_mfma_f32_16x16x32_bf16 v[52:55], v[176:179], v[184:187], 0
	v_mfma_f32_16x16x32_bf16 v[44:47], v[168:171], v[192:195], 0
	v_mfma_f32_16x16x32_bf16 v[36:39], v[176:179], v[192:195], 0
	v_mfma_f32_16x16x32_bf16 v[28:31], v[168:171], v[212:215], 0
	v_mfma_f32_16x16x32_bf16 v[20:23], v[176:179], v[212:215], 0
	v_mfma_f32_16x16x32_bf16 v[12:15], v[168:171], v[220:223], 0
	v_mfma_f32_16x16x32_bf16 v[4:7], v[176:179], v[220:223], 0
	v_mfma_f32_16x16x32_bf16 v[60:63], v[172:175], v[188:191], v[60:63]
	v_mfma_f32_16x16x32_bf16 v[52:55], v[180:183], v[188:191], v[52:55]
	v_mfma_f32_16x16x32_bf16 v[44:47], v[172:175], v[196:199], v[44:47]
	v_mfma_f32_16x16x32_bf16 v[36:39], v[180:183], v[196:199], v[36:39]
	v_mfma_f32_16x16x32_bf16 v[28:31], v[172:175], v[216:219], v[28:31]
	v_mfma_f32_16x16x32_bf16 v[20:23], v[180:183], v[216:219], v[20:23]
	v_mfma_f32_16x16x32_bf16 v[12:15], v[172:175], v[224:227], v[12:15]
	v_mfma_f32_16x16x32_bf16 v[4:7], v[180:183], v[224:227], v[4:7]
	s_setprio 0
	s_barrier
	s_add_i32 s63, 0, 0x18000
	v_add_u32_e32 v155, s63, v151
	s_add_i32 s68, 0, 0x1c000
	ds_read_b128 v[144:147], v155
	ds_read_b128 v[156:159], v155 offset:1024
	ds_read_b128 v[160:163], v155 offset:2048
	ds_read_b128 v[164:167], v155 offset:3072
	v_add_u32_e32 v155, s68, v151
	ds_read_b128 v[168:171], v155
	ds_read_b128 v[172:175], v155 offset:1024
	ds_read_b128 v[176:179], v155 offset:2048
	ds_read_b128 v[180:183], v155 offset:3072
	s_add_u32 s36, s36, 0x40000
	s_addc_u32 s37, s37, 0
	s_mov_b32 m0, s48
	v_lshl_add_u64 v[228:229], s[36:37], 0, v[138:139]
	ds_read_b128 v[184:187], v154 offset:32768
	ds_read_b128 v[188:191], v154 offset:33792
	ds_read_b128 v[192:195], v154 offset:34816
	ds_read_b128 v[196:199], v154 offset:35840
	ds_read_b128 v[212:215], v154 offset:36864
	ds_read_b128 v[216:219], v154 offset:37888
	ds_read_b128 v[220:223], v154 offset:38912
	ds_read_b128 v[224:227], v154 offset:39936
	global_load_lds_dwordx4 v[228:229], off
	v_lshl_add_u64 v[228:229], s[36:37], 0, v[134:135]
	s_mov_b32 m0, s49
	s_nop 0
	global_load_lds_dwordx4 v[228:229], off
	s_waitcnt vmcnt(8)
	s_waitcnt lgkmcnt(0)
	s_barrier
	s_setprio 1
	s_waitcnt lgkmcnt(0)
	v_mfma_f32_16x16x32_bf16 v[128:131], v[144:147], v[184:187], v[128:131]
	v_mfma_f32_16x16x32_bf16 v[120:123], v[160:163], v[184:187], v[120:123]
	v_mfma_f32_16x16x32_bf16 v[112:115], v[144:147], v[192:195], v[112:115]
	v_mfma_f32_16x16x32_bf16 v[104:107], v[160:163], v[192:195], v[104:107]
	v_mfma_f32_16x16x32_bf16 v[96:99], v[144:147], v[212:215], v[96:99]
	v_mfma_f32_16x16x32_bf16 v[88:91], v[160:163], v[212:215], v[88:91]
	v_mfma_f32_16x16x32_bf16 v[80:83], v[144:147], v[220:223], v[80:83]
	v_mfma_f32_16x16x32_bf16 v[72:75], v[160:163], v[220:223], v[72:75]
	v_mfma_f32_16x16x32_bf16 v[128:131], v[156:159], v[188:191], v[128:131]
	v_mfma_f32_16x16x32_bf16 v[120:123], v[164:167], v[188:191], v[120:123]
	v_mfma_f32_16x16x32_bf16 v[112:115], v[156:159], v[196:199], v[112:115]
	v_mfma_f32_16x16x32_bf16 v[104:107], v[164:167], v[196:199], v[104:107]
	v_mfma_f32_16x16x32_bf16 v[96:99], v[156:159], v[216:219], v[96:99]
	v_mfma_f32_16x16x32_bf16 v[88:91], v[164:167], v[216:219], v[88:91]
	v_mfma_f32_16x16x32_bf16 v[80:83], v[156:159], v[224:227], v[80:83]
	v_mfma_f32_16x16x32_bf16 v[72:75], v[164:167], v[224:227], v[72:75]
	s_setprio 0
	s_setprio 1
	v_mfma_f32_16x16x32_bf16 v[124:127], v[168:171], v[184:187], v[124:127]
	v_mfma_f32_16x16x32_bf16 v[116:119], v[176:179], v[184:187], v[116:119]
	v_mfma_f32_16x16x32_bf16 v[108:111], v[168:171], v[192:195], v[108:111]
	v_mfma_f32_16x16x32_bf16 v[100:103], v[176:179], v[192:195], v[100:103]
	v_mfma_f32_16x16x32_bf16 v[92:95], v[168:171], v[212:215], v[92:95]
	v_mfma_f32_16x16x32_bf16 v[84:87], v[176:179], v[212:215], v[84:87]
	v_mfma_f32_16x16x32_bf16 v[76:79], v[168:171], v[220:223], v[76:79]
	v_mfma_f32_16x16x32_bf16 v[68:71], v[176:179], v[220:223], v[68:71]
	v_mfma_f32_16x16x32_bf16 v[124:127], v[172:175], v[188:191], v[124:127]
	v_mfma_f32_16x16x32_bf16 v[116:119], v[180:183], v[188:191], v[116:119]
	v_mfma_f32_16x16x32_bf16 v[108:111], v[172:175], v[196:199], v[108:111]
	v_mfma_f32_16x16x32_bf16 v[100:103], v[180:183], v[196:199], v[100:103]
	v_mfma_f32_16x16x32_bf16 v[92:95], v[172:175], v[216:219], v[92:95]
	v_mfma_f32_16x16x32_bf16 v[84:87], v[180:183], v[216:219], v[84:87]
	v_mfma_f32_16x16x32_bf16 v[76:79], v[172:175], v[224:227], v[76:79]
	v_mfma_f32_16x16x32_bf16 v[68:71], v[180:183], v[224:227], v[68:71]
	s_setprio 0
	s_barrier
; #define PG8_STAGE(bufoff, gbase, voff) do { _Pragma("unroll") for (int _i = 0; _i < 2; ++_i) \
;         __builtin_amdgcn_global_load_lds((const unsigned*)((const char*)(gbase) + (voff)[_i]), (PG8_LAS unsigned*)(lds + (bufoff) + ldsw + _i * 8192), 16, 0, 0); } while (0)
; #define PG8_LDA(dst, b, h) do { _Pragma("unroll") for (int m = 0; m < 4; ++m) _Pragma("unroll") for (int k = 0; k < 2; ++k) dst[m][k] = *(const PG8_LAS bf16x8*)(lds + PG8_SA(b, h) + aoff + m * 2048 + k * 1024); } while (0)
; #define PG8_MMA(ai, bj, At, Bt) do { __builtin_amdgcn_s_setprio(1); _Pragma("unroll") for (int m = 0; m < 4; ++m) _Pragma("unroll") for (int n = 0; n < 2; ++n) _Pragma("unroll") for (int k = 0; k < 2; ++k) \
;         acc[ai][bj][m][n] = __builtin_amdgcn_mfma_f32_16x16x32_bf16(Bt[n][k], At[m][k], acc[ai][bj][m][n], 0, 0, 0); __builtin_amdgcn_s_setprio(0); } while (0)
; #define PG8_WAIT_V(n) asm volatile("s_waitcnt vmcnt(" #n ")" ::: "memory")
; #define PG8_WAIT_L(n) asm volatile("s_waitcnt lgkmcnt(" #n ")" ::: "memory")
; #define PG8_BAR __builtin_amdgcn_s_barrier()
; #define PG8_SCHED __builtin_amdgcn_sched_barrier(0)
; template <class Epi, class Sched, bool ALIGN_EPI = false, bool SP2 = false>
; __device__ __forceinline__ void gemm_phase(PG8_LAS unsigned char* lds, const Gemm g, const Sched& S, const Epi& E, const int tid) {
;     ...
;             PG8_WAIT_V(8); PG8_WAIT_L(0); PG8_BAR; PG8_MMA(0, 0, At, B0); PG8_MMA(0, 1, At, B1); PG8_BAR; PG8_SCHED;
;             PG8_LDA(At, 1, 1); PG8_STAGE(PG8_SB(1, 0), b3, voffB); PG8_STAGE(PG8_SB(1, 1), b3, voffB1); PG8_STAGE(PG8_SA(1, 0), a3, voffA);
;             PG8_WAIT_V(8); PG8_WAIT_L(0); PG8_BAR; PG8_MMA(1, 0, At, B0); PG8_MMA(1, 1, At, B1); PG8_BAR; PG8_SCHED;
	s_add_i32 s36, s63, s33
	v_lshl_add_u64 v[148:149], v[148:149], 0, s[66:67]
	s_mov_b32 m0, s36
	ds_read_b128 v[184:187], v154 offset:49152
	ds_read_b128 v[188:191], v154 offset:50176
	ds_read_b128 v[192:195], v154 offset:51200
	ds_read_b128 v[196:199], v154 offset:52224
	ds_read_b128 v[212:215], v154 offset:53248
	ds_read_b128 v[216:219], v154 offset:54272
	ds_read_b128 v[220:223], v154 offset:55296
	ds_read_b128 v[224:227], v154 offset:56320
	global_load_lds_dwordx4 v[148:149], off
	v_lshl_add_u64 v[148:149], v[200:201], 0, s[66:67]
	s_add_i32 m0, s36, 0x2000
	s_add_i32 s36, s68, s33
	global_load_lds_dwordx4 v[148:149], off
	v_lshl_add_u64 v[148:149], v[202:203], 0, s[66:67]
	s_mov_b32 m0, s36
	s_nop 0
	global_load_lds_dwordx4 v[148:149], off
	v_lshl_add_u64 v[148:149], v[204:205], 0, s[66:67]
	s_add_i32 m0, s36, 0x2000
	s_nop 0
	global_load_lds_dwordx4 v[148:149], off
	v_lshl_add_u64 v[148:149], v[208:209], 0, s[66:67]
	s_mov_b32 m0, s50
	s_nop 0
	global_load_lds_dwordx4 v[148:149], off
	v_lshl_add_u64 v[148:149], v[210:211], 0, s[66:67]
	s_mov_b32 m0, s51
	s_nop 0
	global_load_lds_dwordx4 v[148:149], off
	s_waitcnt vmcnt(8)
	s_waitcnt lgkmcnt(0)
	s_barrier
	s_setprio 1
	s_waitcnt lgkmcnt(0)
	v_mfma_f32_16x16x32_bf16 v[64:67], v[144:147], v[184:187], v[64:67]
	v_mfma_f32_16x16x32_bf16 v[56:59], v[160:163], v[184:187], v[56:59]
	v_mfma_f32_16x16x32_bf16 v[48:51], v[144:147], v[192:195], v[48:51]
	v_mfma_f32_16x16x32_bf16 v[40:43], v[160:163], v[192:195], v[40:43]
	v_mfma_f32_16x16x32_bf16 v[32:35], v[144:147], v[212:215], v[32:35]
	v_mfma_f32_16x16x32_bf16 v[24:27], v[160:163], v[212:215], v[24:27]
	v_mfma_f32_16x16x32_bf16 v[16:19], v[144:147], v[220:223], v[16:19]
	v_mfma_f32_16x16x32_bf16 v[8:11], v[160:163], v[220:223], v[8:11]
	v_mfma_f32_16x16x32_bf16 v[64:67], v[156:159], v[188:191], v[64:67]
	v_mfma_f32_16x16x32_bf16 v[56:59], v[164:167], v[188:191], v[56:59]
	v_mfma_f32_16x16x32_bf16 v[48:51], v[156:159], v[196:199], v[48:51]
	v_mfma_f32_16x16x32_bf16 v[40:43], v[164:167], v[196:199], v[40:43]
	v_mfma_f32_16x16x32_bf16 v[32:35], v[156:159], v[216:219], v[32:35]
	v_mfma_f32_16x16x32_bf16 v[24:27], v[164:167], v[216:219], v[24:27]
	v_mfma_f32_16x16x32_bf16 v[16:19], v[156:159], v[224:227], v[16:19]
	v_mfma_f32_16x16x32_bf16 v[8:11], v[164:167], v[224:227], v[8:11]
	s_setprio 0
	s_setprio 1
	v_mfma_f32_16x16x32_bf16 v[60:63], v[168:171], v[184:187], v[60:63]
	v_mfma_f32_16x16x32_bf16 v[52:55], v[176:179], v[184:187], v[52:55]
	v_mfma_f32_16x16x32_bf16 v[44:47], v[168:171], v[192:195], v[44:47]
	v_mfma_f32_16x16x32_bf16 v[36:39], v[176:179], v[192:195], v[36:39]
	v_mfma_f32_16x16x32_bf16 v[28:31], v[168:171], v[212:215], v[28:31]
	v_mfma_f32_16x16x32_bf16 v[20:23], v[176:179], v[212:215], v[20:23]
	v_mfma_f32_16x16x32_bf16 v[12:15], v[168:171], v[220:223], v[12:15]
	v_mfma_f32_16x16x32_bf16 v[4:7], v[176:179], v[220:223], v[4:7]
	v_mfma_f32_16x16x32_bf16 v[60:63], v[172:175], v[188:191], v[60:63]
	v_mfma_f32_16x16x32_bf16 v[52:55], v[180:183], v[188:191], v[52:55]
	v_mfma_f32_16x16x32_bf16 v[44:47], v[172:175], v[196:199], v[44:47]
	v_mfma_f32_16x16x32_bf16 v[36:39], v[180:183], v[196:199], v[36:39]
	v_mfma_f32_16x16x32_bf16 v[28:31], v[172:175], v[216:219], v[28:31]
	v_mfma_f32_16x16x32_bf16 v[20:23], v[180:183], v[216:219], v[20:23]
	v_mfma_f32_16x16x32_bf16 v[12:15], v[172:175], v[224:227], v[12:15]
	v_mfma_f32_16x16x32_bf16 v[4:7], v[180:183], v[224:227], v[4:7]
	s_setprio 0
	s_barrier
	s_add_i32 s62, s62, 2
	s_add_u32 s46, s46, 0x100
	s_addc_u32 s47, s47, 0
	s_add_u32 s52, s52, 0x100
	s_addc_u32 s53, s53, 0
	s_cmp_gt_u32 s62, 13
	s_cbranch_scc1 .Lpeel_done_727

; #define PG8_BAR __builtin_amdgcn_s_barrier()
; template <class Epi, class Sched, bool ALIGN_EPI = false, bool SP2 = false>
; __device__ __forceinline__ void gemm_phase(PG8_LAS unsigned char* lds, const Gemm g, const Sched& S, const Epi& E, const int tid) {
;     ...
;         }
;         if constexpr (ALIGN_EPI) { if (wr == 0) PG8_BAR; }
;         if constexpr (!Epi::AFTER_DRAIN) { E(acc, cur, wr, wc, fr, fq); S.done(cur); }
.Lpeel_done_727:
	s_and_b64 vcc, exec, s[6:7]
	s_cbranch_vccz .LBB0_730
	s_barrier
